# speedup vs baseline: 1.0033x; 1.0033x over previous
.LBB3_36:
	s_andn2_b64 vcc, exec, s[6:7]
	s_cbranch_vccnz .LBB3_86
	s_cmpk_gt_u32 s2, 0xff
	s_cbranch_scc1 .LBB3_86
	s_mov_b64 s[40:41], s[0:1]
	s_mov_b32 s44, s18
	s_mov_b32 s45, s19
	s_mov_b32 s46, 0
	s_mov_b32 s60, s2
	s_mov_b32 s61, 0
	s_mov_b32 s65, 0
	s_mov_b32 s73, 0
	v_readfirstlane_b32 s72, v0
	s_load_dwordx2 s[68:69], s[0:1], 0x0
	s_load_dwordx2 s[70:71], s[0:1], 0x38
	s_mov_b32 s49, 0
	s_mov_b32 s47, 0
	s_mov_b32 s48, 0
	s_movk_i32 s50, 0x63
	s_load_dwordx2 s[52:53], s[0:1], 0x30
	s_add_i32 s51, s19, 31
	s_lshr_b32 s51, s51, 5
	s_sub_i32 s51, s51, 0x200
	s_sub_i32 s55, s51, 1
	s_cmp_lt_u32 s55, 0x80
	s_cselect_b32 s51, s51, 0
	v_mov_b32_e32 v248, v0
.Lgru_tile:
	s_cmp_eq_u32 s47, 1
	s_cselect_b32 s67, 10, 21
	s_cmp_lg_u32 s46, 0
	s_cbranch_scc1 .Lgru_tile_alt
	s_load_dwordx8 s[8:15], s[0:1], 0x0
	s_load_dwordx2 s[2:3], s[0:1], 0x20
	v_lshlrev_b32_e32 v52, 4, v0
	v_mov_b32_e32 v53, 0
	s_movk_i32 s6, 0x100
	s_waitcnt lgkmcnt(0)
	v_lshl_add_u64 v[30:31], s[14:15], 0, v[52:53]
	v_add_co_u32_e32 v14, vcc, 0x2000, v30
	v_bfe_u32 v55, v0, 6, 2
	s_nop 0
	v_addc_co_u32_e32 v15, vcc, 0, v31, vcc
	v_add_co_u32_e32 v22, vcc, 0x6000, v30
	v_mov_b32_e32 v46, s3
	s_nop 0
	v_addc_co_u32_e32 v23, vcc, 0, v31, vcc
	v_add_co_u32_e32 v32, vcc, 0xa000, v30
	v_mov_b32_e32 v47, s13
	s_nop 0
	v_addc_co_u32_e32 v33, vcc, 0, v31, vcc
	v_add_co_u32_e32 v38, vcc, 0xe000, v30
	v_mov_b32_e32 v48, s12
	s_nop 0
	v_addc_co_u32_e32 v39, vcc, 0, v31, vcc
	v_cmp_gt_u32_e32 vcc, s6, v0
	v_mul_u32_u24_e32 v54, 0x540, v55
	v_mov_b32_e32 v49, v53
	v_cndmask_b32_e32 v47, v46, v47, vcc
	v_mov_b32_e32 v46, s2
	v_cndmask_b32_e32 v46, v46, v48, vcc
	v_lshlrev_b32_e32 v48, 4, v54
	v_lshl_add_u64 v[46:47], v[46:47], 0, v[48:49]
	v_lshlrev_b32_e32 v50, 4, v1
	v_mov_b32_e32 v51, v53
	s_movk_i32 s5, 0x1000
	v_lshl_add_u64 v[46:47], v[46:47], 0, v[50:51]
	v_add_co_u32_e32 v48, vcc, s5, v46
	s_movk_i32 s4, 0x2000
	s_nop 0
	v_addc_co_u32_e32 v49, vcc, 0, v47, vcc
	v_or_b32_e32 v56, 0x400, v0
	v_add_co_u32_e32 v60, vcc, s4, v46
	v_lshlrev_b32_e32 v16, 4, v56
	v_or_b32_e32 v24, 0x8000, v52
	v_or_b32_e32 v34, 0xc000, v52
	v_or_b32_e32 v30, 0x1000, v0
	v_addc_co_u32_e32 v61, vcc, 0, v47, vcc
	s_movk_i32 s2, 0x3000
	global_load_dwordx4 v[2:5], v52, s[14:15]
	global_load_dwordx4 v[6:9], v[14:15], off
	global_load_dwordx4 v[10:13], v16, s[14:15]
	s_nop 0
	global_load_dwordx4 v[14:17], v[22:23], off
	global_load_dwordx4 v[18:21], v24, s[14:15]
	s_nop 0
	global_load_dwordx4 v[22:25], v[32:33], off
	global_load_dwordx4 v[26:29], v34, s[14:15]
	v_lshlrev_b32_e32 v57, 4, v30
	global_load_dwordx4 v[30:33], v[38:39], off
	global_load_dwordx4 v[34:37], v57, s[14:15]
	v_or_b32_e32 v38, 0x1200, v0
	v_add_co_u32_e32 v62, vcc, s2, v46
	v_lshlrev_b32_e32 v58, 4, v38
	v_or_b32_e32 v38, 0x1400, v0
	v_addc_co_u32_e32 v63, vcc, 0, v47, vcc
	s_movk_i32 s2, 0x4000
	v_min_u32_e32 v38, 0x14ff, v38
	v_add_co_u32_e32 v64, vcc, s2, v46
	v_lshlrev_b32_e32 v59, 4, v38
	global_load_dwordx4 v[38:41], v58, s[14:15]
	global_load_dwordx4 v[42:45], v59, s[14:15]
	global_load_dwordx4 v[82:85], v[46:47], off
	global_load_dwordx4 v[86:89], v[46:47], off offset:1024
	global_load_dwordx4 v[90:93], v[46:47], off offset:2048
	global_load_dwordx4 v[94:97], v[46:47], off offset:3072
	global_load_dwordx4 v[98:101], v[48:49], off offset:1024
	global_load_dwordx4 v[102:105], v[48:49], off offset:2048
	global_load_dwordx4 v[106:109], v[60:61], off offset:-4096
	global_load_dwordx4 v[110:113], v[60:61], off
	global_load_dwordx4 v[114:117], v[60:61], off offset:1024
	global_load_dwordx4 v[118:121], v[60:61], off offset:2048
	v_addc_co_u32_e32 v65, vcc, 0, v47, vcc
	global_load_dwordx4 v[122:125], v[60:61], off offset:3072
	global_load_dwordx4 v[126:129], v[64:65], off offset:-4096
	global_load_dwordx4 v[130:133], v[48:49], off offset:3072
	global_load_dwordx4 v[134:137], v[62:63], off offset:1024
	global_load_dwordx4 v[138:141], v[62:63], off offset:2048
	global_load_dwordx4 v[142:145], v[62:63], off offset:3072
	global_load_dwordx4 v[146:149], v[64:65], off
	global_load_dwordx4 v[150:153], v[64:65], off offset:1024
	global_load_dwordx4 v[154:157], v[64:65], off offset:2048
	global_load_dwordx4 v[158:161], v[64:65], off offset:3072
	v_add_co_u32_e32 v46, vcc, 0x5000, v46
	s_movk_i32 s2, 0xff
	s_nop 0
	v_addc_co_u32_e32 v47, vcc, 0, v47, vcc
	global_load_dwordx4 v[162:165], v[46:47], off
.Lgru_after_wloads:
	v_cmp_lt_u32_e64 s[6:7], s2, v0
	v_cmp_gt_u32_e32 vcc, 32, v0
	s_and_saveexec_b64 s[2:3], vcc
	s_cbranch_execz .LBB3_43
	s_cmp_eq_u32 s65, 0
	s_cbranch_scc1 .Lpf_tl_normal
	v_mov_b32_e32 v47, v251
	s_mov_b64 s[4:5], exec
	s_branch .LBB3_42
.Lpf_tl_normal:
	v_or_b32_e32 v46, s18, v0
	v_cmp_gt_i32_e32 vcc, s19, v46
	v_mov_b32_e32 v47, -1
	s_and_saveexec_b64 s[4:5], vcc
	s_cbranch_execz .LBB3_42
	s_movk_i32 s12, 0xf9f
	v_cmp_lt_i32_e32 vcc, s12, v46
	s_and_saveexec_b64 s[12:13], vcc
	s_cbranch_execz .LBB3_41
	s_load_dwordx2 s[14:15], s[0:1], 0x38
	v_mov_b32_e32 v47, 0
	s_waitcnt lgkmcnt(0)
	v_lshl_add_u64 v[46:47], v[46:47], 2, s[14:15]
	v_add_co_u32_e32 v46, vcc, 0xffffd000, v46
	s_nop 1
	v_addc_co_u32_e32 v47, vcc, -1, v47, vcc
	global_load_dword v46, v[46:47], off offset:-3712

.LBB3_43:
	s_or_b64 exec, exec, s[2:3]
	v_min_u32_e32 v46, 0x11f, v0
	v_or_b32_e32 v51, 0x200, v46
	v_mul_u32_u24_e32 v46, 0xa3e, v0
	v_lshrrev_b32_e32 v49, 16, v46
	v_mov_b32_e32 v47, 0x27280
	v_mul_u32_u24_e32 v48, 0xa3e, v51
	v_lshl_or_b32 v46, v49, 2, v47
	v_lshrrev_b32_e32 v48, 16, v48
	s_waitcnt lgkmcnt(0)
	s_barrier
	ds_read_b32 v46, v46
	v_lshl_add_u32 v47, v48, 2, v47
	s_load_dwordx2 s[0:1], s[0:1], 0x28
	ds_read_b32 v60, v47
	s_movk_i32 s4, 0xa3e
	s_waitcnt lgkmcnt(0)
	s_cmp_eq_u32 s65, 0
	s_cbranch_scc1 .Lpf_tk_normal
	v_mov_b32_e32 v46, -1
	v_mov_b32_e32 v60, -1
.Lpf_tk_normal:
	v_cmp_lt_i32_e32 vcc, -1, v46
	v_mov_b32_e32 v53, 0
	s_and_saveexec_b64 s[2:3], vcc
	s_cbranch_execz .LBB3_45
	v_mul_u32_u24_sdwa v47, v0, s4 dst_sel:DWORD dst_unused:UNUSED_PAD src0_sel:WORD_0 src1_sel:DWORD
	v_mov_b32_e32 v53, 25
	v_mul_lo_u16_sdwa v47, v47, v53 dst_sel:DWORD dst_unused:UNUSED_PAD src0_sel:WORD_1 src1_sel:DWORD
	v_sub_u16_e32 v62, v0, v47
	v_mad_u64_u32 v[46:47], s[4:5], v46, 25, v[62:63]
	v_mov_b32_e32 v47, 0
	v_lshl_add_u64 v[46:47], v[46:47], 2, s[8:9]
	global_load_dword v53, v[46:47], off

.LBB3_49:
	s_or_b64 exec, exec, s[2:3]
	s_movk_i32 s2, 0xa3e
	v_mul_u32_u24_sdwa v60, v0, s2 dst_sel:DWORD dst_unused:UNUSED_PAD src0_sel:WORD_0 src1_sel:DWORD
	v_mov_b32_e32 v62, 25
	v_mul_lo_u16_sdwa v60, v60, v62 dst_sel:DWORD dst_unused:UNUSED_PAD src0_sel:WORD_1 src1_sel:DWORD
	v_sub_u16_e32 v60, v0, v60
	v_mul_u32_u24_e32 v49, 0x64, v49
	v_lshlrev_b32_e32 v60, 2, v60
	s_mov_b32 s2, 0x25600
	v_mul_u32_u24_e32 v48, 0x64, v48
	v_lshlrev_b32_e32 v46, 2, v46
	v_add3_u32 v49, v49, v60, s2
	v_add3_u32 v46, v48, v46, s2
	s_movk_i32 s4, 0xeeef
	v_mov_b32_e32 v60, 0x3333
	s_cmp_eq_u32 s65, 0
	s_cbranch_scc1 .Lpf_wr_normal
	v_mov_b32_e32 v53, v249
	v_mov_b32_e32 v61, v250
	s_mov_b32 s65, 0
	s_branch .Lpf_wr
.Lpf_wr_normal:
	s_waitcnt vmcnt(0)
.Lpf_wr:
	ds_write_b32 v49, v53
	ds_write_b32 v46, v61
	v_mad_legacy_u16 v46, v0, s4, v60
	s_movk_i32 s5, 0x1111
	v_bfrev_b32_e32 v62, 60
	v_cmp_gt_u16_e32 vcc, s5, v46
	s_movk_i32 s2, 0x3a0
	v_or_b32_e32 v51, 0x200, v0
	v_add_u32_e32 v61, 0x1fc00, v52
	v_add_u32_e32 v53, 0x23800, v52
	v_cndmask_b32_e32 v46, 0, v62, vcc
	v_mov_b32_e32 v48, v47
	v_mov_b32_e32 v49, v47
	v_cmp_gt_u32_e32 vcc, s2, v0
	ds_write_b128 v61, v[46:49]
	s_and_saveexec_b64 s[2:3], vcc
	s_cbranch_execz .LBB3_51
	s_movk_i32 s8, 0x1c0
	v_add_u32_e32 v46, 0x2000, v61
	v_add_u32_e32 v47, 0xffffe400, v53
	v_cmp_gt_u32_e32 vcc, s8, v0
	s_nop 1
	v_cndmask_b32_e32 v61, v47, v46, vcc
	v_mad_legacy_u16 v46, v51, s4, v60
	v_cmp_gt_u16_e32 vcc, s5, v46
	v_mov_b32_e32 v47, 0
	v_mov_b32_e32 v48, v47
	v_cndmask_b32_e32 v46, 0, v62, vcc
	v_mov_b32_e32 v49, v47
	ds_write_b128 v61, v[46:49]

.LBB3_57:
	s_or_b64 exec, exec, s[4:5]
	s_movk_i32 s4, 0x619
	v_mul_u32_u24_sdwa v3, v0, s4 dst_sel:DWORD dst_unused:UNUSED_PAD src0_sel:WORD_0 src1_sel:DWORD
	v_lshrrev_b32_e32 v3, 16, v3
	v_mul_lo_u16_e32 v4, 42, v3
	v_sub_u16_e32 v6, v0, v4
	s_movk_i32 s4, 0x64
	v_mov_b32_e32 v4, 0x25600
	v_add_u32_e32 v4, s48, v4
	v_mad_u32_u24 v5, v3, s4, v4
	v_mul_u32_u24_e32 v7, 0x619, v51
	v_min_u32_e32 v19, 0x53f, v56
	s_waitcnt lgkmcnt(0)
	s_barrier
	s_cmp_eq_u32 s61, 0
	s_cbranch_scc1 .Lgru_noflag
	s_waitcnt vmcnt(0)
	s_barrier
	v_readfirstlane_b32 s55, v248
	s_nop 3
	s_cmp_lg_u32 s55, 0
	s_cbranch_scc1 .Lgru_noflag_clear
	v_mov_b32_e32 v224, s61
	v_mov_b32_e32 v225, 1
	global_store_byte v224, v225, s[52:53] offset:11 sc0 sc1

.LBB3_62:
	s_or_b64 exec, exec, s[0:1]
	s_sub_i32 s66, s14, s67
	s_cmp_gt_u32 s66, 3
	s_cbranch_scc1 .Lpf_done
	s_cmp_eq_u32 s66, 0
	s_cbranch_scc1 .Lpf_0
	s_cmp_eq_u32 s73, 0
	s_cbranch_scc1 .Lpf_done
	s_cmp_eq_u32 s66, 1
	s_cbranch_scc1 .Lpf_1
	s_cmp_eq_u32 s66, 2
	s_cbranch_scc1 .Lpf_2
	s_waitcnt vmcnt(0)
.Lpf_done:
	s_add_i32 s14, s14, 1
	s_cmp_eq_u32 s14, 27
	s_waitcnt lgkmcnt(0)
	s_barrier
	s_cbranch_scc1 .LBB3_83

.Lgru_next_tile:
	s_mov_b32 s65, s73
	s_mov_b32 s73, 0
	s_mov_b64 exec, -1
	s_mov_b32 s46, 1
	s_mov_b64 s[0:1], s[40:41]
	s_mov_b32 s18, s44
	s_mov_b32 s19, s45
	v_mov_b32_e32 v0, v248
	v_and_b32_e32 v1, 63, v0
	v_lshrrev_b32_e32 v195, 6, v0
	s_waitcnt lgkmcnt(0)
	s_barrier
	s_branch .Lgru_tile

.Lpf_0:
	s_mov_b32 s62, -1
	s_cmp_lg_u32 s51, 0
	s_cbranch_scc1 .Lpfs_split
	s_add_i32 s66, s44, 0x2000
	s_cmp_lt_i32 s66, s45
	s_cselect_b32 s62, s66, -1
	s_branch .Lpfs_done
.Lpfs_split:
	s_cmp_gt_u32 s49, 1
	s_cbranch_scc1 .Lpfs_done
	s_add_i32 s62, s60, 0x100
	s_lshl_b32 s62, s62, 5
	s_cmp_eq_u32 s49, 1
	s_cbranch_scc1 .Lpfs_j2
	s_cmp_ge_u32 s60, s51
	s_cbranch_scc1 .Lpfs_done
	s_add_i32 s62, s60, 0x200
	s_lshl_b32 s62, s62, 5
	s_branch .Lpfs_done
.Lpfs_j2:
	s_cmp_lt_u32 s60, s51
	s_cbranch_scc1 .Lpfs_done
	s_lshl_b32 s66, s51, 1
	s_cmp_ge_u32 s60, s66
	s_cbranch_scc1 .Lpfs_none
	s_sub_i32 s62, s60, s51
	s_add_i32 s62, s62, 0x200
	s_lshl_b32 s62, s62, 5
	s_branch .Lpfs_done
.Lpfs_none:
	s_mov_b32 s62, -1
.Lpfs_done:
	s_cmp_lt_i32 s62, 0
	s_cbranch_scc1 .Lpf_done
	s_mov_b32 s73, 1
	s_cmp_lg_u32 s72, 0
	s_cbranch_scc1 .Lpf_done
	s_add_u32 s76, s70, 0xffffc180
	s_addc_u32 s77, s71, -1
	v_and_b32_e32 v219, 63, v248
	v_add_u32_e32 v220, s62, v219
	v_mov_b32_e32 v251, -1
	v_cmp_gt_i32_e32 vcc, s45, v220
	v_cmp_gt_u32_e64 s[74:75], 32, v219
	s_and_b64 vcc, vcc, s[74:75]
	s_and_saveexec_b64 s[74:75], vcc
	s_cbranch_execz .Lpf0_skip
	v_lshlrev_b32_e32 v220, 2, v220
	global_load_dword v251, v220, s[76:77]
.Lpf0_skip:
	s_or_b64 exec, exec, s[74:75]
	s_branch .Lpf_done
.Lpf_1:
	s_cmp_lg_u32 s72, 0
	s_cbranch_scc1 .Lpf_done
	v_and_b32_e32 v219, 63, v248
	v_mov_b32_e32 v220, 0x27340
	v_lshl_add_u32 v220, v219, 2, v220
	s_waitcnt vmcnt(0)
	ds_write_b32 v220, v251
	s_branch .Lpf_done
.Lpf_2:
	v_mul_u32_u24_e32 v219, 0xa3e, v248
	v_lshrrev_b32_e32 v219, 16, v219
	v_min_u32_e32 v220, 0x11f, v248
	v_or_b32_e32 v220, 0x200, v220
	v_mul_u32_u24_e32 v221, 0xa3e, v220
	v_lshrrev_b32_e32 v221, 16, v221
	v_mov_b32_e32 v222, 0x27340
	v_lshl_add_u32 v223, v219, 2, v222
	v_lshl_add_u32 v224, v221, 2, v222
	ds_read_b32 v223, v223
	ds_read_b32 v224, v224
	v_mul_u32_u24_e32 v219, 25, v219
	v_sub_u32_e32 v219, v248, v219
	v_mul_u32_u24_e32 v221, 25, v221
	v_sub_u32_e32 v221, v220, v221
	v_mov_b32_e32 v249, 0
	v_mov_b32_e32 v250, 0
	s_waitcnt lgkmcnt(0)
	v_cmp_lt_i32_e32 vcc, -1, v223
	s_and_saveexec_b64 s[74:75], vcc
	s_cbranch_execz .Lpf2_a
	v_mad_u32_u24 v225, v223, 25, v219
	v_lshlrev_b32_e32 v225, 2, v225
	global_load_dword v249, v225, s[68:69]
.Lpf2_a:
	s_or_b64 exec, exec, s[74:75]
	v_cmp_lt_i32_e32 vcc, -1, v224
	s_and_saveexec_b64 s[74:75], vcc
	s_cbranch_execz .Lpf2_b
	v_mad_u32_u24 v225, v224, 25, v221
	v_lshlrev_b32_e32 v225, 2, v225
	global_load_dword v250, v225, s[68:69]

	.amdhsa_kernel _Z8gru_mfmaPKiPKDF16_PKDv8_DF16_S5_S5_S5_S0_S0_PfPKfS8_S8_S8_S0_
		.amdhsa_group_segment_fixed_size 160832
		.amdhsa_private_segment_fixed_size 0
		.amdhsa_kernarg_size 112
		.amdhsa_user_sgpr_count 2
		.amdhsa_user_sgpr_dispatch_ptr 0
		.amdhsa_user_sgpr_queue_ptr 0
		.amdhsa_user_sgpr_kernarg_segment_ptr 1
		.amdhsa_user_sgpr_dispatch_id 0
		.amdhsa_user_sgpr_kernarg_preload_length 0
		.amdhsa_user_sgpr_kernarg_preload_offset 0
		.amdhsa_user_sgpr_private_segment_size 0
		.amdhsa_uses_dynamic_stack 0
		.amdhsa_enable_private_segment 0
		.amdhsa_system_sgpr_workgroup_id_x 1
		.amdhsa_system_sgpr_workgroup_id_y 0
		.amdhsa_system_sgpr_workgroup_id_z 0
		.amdhsa_system_sgpr_workgroup_info 0
		.amdhsa_system_vgpr_workitem_id 0
		.amdhsa_next_free_vgpr 256
		.amdhsa_next_free_sgpr 96
		.amdhsa_accum_offset 256
		.amdhsa_reserve_vcc 1
		.amdhsa_float_round_mode_32 0
		.amdhsa_float_round_mode_16_64 0
		.amdhsa_float_denorm_mode_32 3
		.amdhsa_float_denorm_mode_16_64 3
		.amdhsa_dx10_clamp 1
		.amdhsa_ieee_mode 1
		.amdhsa_fp16_overflow 0
		.amdhsa_tg_split 0
		.amdhsa_exception_fp_ieee_invalid_op 0
		.amdhsa_exception_fp_denorm_src 0
		.amdhsa_exception_fp_ieee_div_zero 0
		.amdhsa_exception_fp_ieee_overflow 0
		.amdhsa_exception_fp_ieee_underflow 0
		.amdhsa_exception_fp_ieee_inexact 0
		.amdhsa_exception_int_div_zero 0
	.end_amdhsa_kernel

amdhsa.kernels:
  - .agpr_count:     0
    .args:
      - .actual_access:  write_only
        .address_space:  global
        .offset:         0
        .size:           8
        .value_kind:     global_buffer
      - .offset:         8
        .size:           4
        .value_kind:     by_value
      - .offset:         16
        .size:           4
        .value_kind:     hidden_block_count_x
      - .offset:         20
        .size:           4
        .value_kind:     hidden_block_count_y
      - .offset:         24
        .size:           4
        .value_kind:     hidden_block_count_z
      - .offset:         28
        .size:           2
        .value_kind:     hidden_group_size_x
      - .offset:         30
        .size:           2
        .value_kind:     hidden_group_size_y
      - .offset:         32
        .size:           2
        .value_kind:     hidden_group_size_z
      - .offset:         34
        .size:           2
        .value_kind:     hidden_remainder_x
      - .offset:         36
        .size:           2
        .value_kind:     hidden_remainder_y
      - .offset:         38
        .size:           2
        .value_kind:     hidden_remainder_z
      - .offset:         56
        .size:           8
        .value_kind:     hidden_global_offset_x
      - .offset:         64
        .size:           8
        .value_kind:     hidden_global_offset_y
      - .offset:         72
        .size:           8
        .value_kind:     hidden_global_offset_z
      - .offset:         80
        .size:           2
        .value_kind:     hidden_grid_dims
    .group_segment_fixed_size: 0
    .kernarg_segment_align: 8
    .kernarg_segment_size: 272
    .language:       OpenCL C
    .language_version:
      - 2
      - 0
    .max_flat_workgroup_size: 1024
    .name:           _Z11zero_kernelPDv4_fi
    .private_segment_fixed_size: 0
    .sgpr_count:     11
    .sgpr_spill_count: 0
    .symbol:         _Z11zero_kernelPDv4_fi.kd
    .uniform_work_group_size: 1
    .uses_dynamic_stack: false
    .vgpr_count:     6
    .vgpr_spill_count: 0
    .wavefront_size: 64
  - .agpr_count:     0
    .args:
      - .actual_access:  read_only
        .address_space:  global
        .offset:         0
        .size:           8
        .value_kind:     global_buffer
      - .actual_access:  read_only
        .address_space:  global
        .offset:         8
        .size:           8
        .value_kind:     global_buffer
      - .actual_access:  read_only
        .address_space:  global
        .offset:         16
        .size:           8
        .value_kind:     global_buffer
      - .actual_access:  read_only
        .address_space:  global
        .offset:         24
        .size:           8
        .value_kind:     global_buffer
      - .actual_access:  write_only
        .address_space:  global
        .offset:         32
        .size:           8
        .value_kind:     global_buffer
      - .actual_access:  read_only
        .address_space:  global
        .offset:         40
        .size:           8
        .value_kind:     global_buffer
      - .actual_access:  read_only
        .address_space:  global
        .offset:         48
        .size:           8
        .value_kind:     global_buffer
      - .address_space:  global
        .offset:         56
        .size:           8
        .value_kind:     global_buffer
      - .address_space:  global
        .offset:         64
        .size:           8
        .value_kind:     global_buffer
      - .address_space:  global
        .offset:         72
        .size:           8
        .value_kind:     global_buffer
      - .address_space:  global
        .offset:         80
        .size:           8
        .value_kind:     global_buffer
      - .offset:         88
        .size:           4
        .value_kind:     hidden_block_count_x
      - .offset:         92
        .size:           4
        .value_kind:     hidden_block_count_y
      - .offset:         96
        .size:           4
        .value_kind:     hidden_block_count_z
      - .offset:         100
        .size:           2
        .value_kind:     hidden_group_size_x
      - .offset:         102
        .size:           2
        .value_kind:     hidden_group_size_y
      - .offset:         104
        .size:           2
        .value_kind:     hidden_group_size_z
      - .offset:         106
        .size:           2
        .value_kind:     hidden_remainder_x
      - .offset:         108
        .size:           2
        .value_kind:     hidden_remainder_y
      - .offset:         110
        .size:           2
        .value_kind:     hidden_remainder_z
      - .offset:         128
        .size:           8
        .value_kind:     hidden_global_offset_x
      - .offset:         136
        .size:           8
        .value_kind:     hidden_global_offset_y
      - .offset:         144
        .size:           8
        .value_kind:     hidden_global_offset_z
      - .offset:         152
        .size:           2
        .value_kind:     hidden_grid_dims
    .group_segment_fixed_size: 61528
    .kernarg_segment_align: 8
    .kernarg_segment_size: 344
    .language:       OpenCL C
    .language_version:
      - 2
      - 0
    .max_flat_workgroup_size: 640
    .name:           _Z11p_gemm_mfmaPKfPKDv8_DF16_S0_S0_PDF16_PKiS6_PiS7_S7_S7_
    .private_segment_fixed_size: 0
    .sgpr_count:     36
    .sgpr_spill_count: 0
    .symbol:         _Z11p_gemm_mfmaPKfPKDv8_DF16_S0_S0_PDF16_PKiS6_PiS7_S7_S7_.kd
    .uniform_work_group_size: 1
    .uses_dynamic_stack: false
    .vgpr_count:     156
    .vgpr_spill_count: 0
    .wavefront_size: 64
  - .agpr_count:     0
    .args:
      - .actual_access:  read_only
        .address_space:  global
        .offset:         0
        .size:           8
        .value_kind:     global_buffer
      - .actual_access:  read_only
        .address_space:  global
        .offset:         8
        .size:           8
        .value_kind:     global_buffer
      - .actual_access:  read_only
        .address_space:  global
        .offset:         16
        .size:           8
        .value_kind:     global_buffer
      - .actual_access:  read_only
        .address_space:  global
        .offset:         24
        .size:           8
        .value_kind:     global_buffer
      - .actual_access:  read_only
        .address_space:  global
        .offset:         32
        .size:           8
        .value_kind:     global_buffer
      - .actual_access:  read_only
        .address_space:  global
        .offset:         40
        .size:           8
        .value_kind:     global_buffer
      - .actual_access:  read_only
        .address_space:  global
        .offset:         48
        .size:           8
        .value_kind:     global_buffer
      - .actual_access:  write_only
        .address_space:  global
        .offset:         56
        .size:           8
        .value_kind:     global_buffer
      - .actual_access:  write_only
        .address_space:  global
        .offset:         64
        .size:           8
        .value_kind:     global_buffer
      - .actual_access:  write_only
        .address_space:  global
        .offset:         72
        .size:           8
        .value_kind:     global_buffer
      - .actual_access:  write_only
        .address_space:  global
        .offset:         80
        .size:           8
        .value_kind:     global_buffer
      - .actual_access:  read_only
        .address_space:  global
        .offset:         88
        .size:           8
        .value_kind:     global_buffer
      - .actual_access:  write_only
        .address_space:  global
        .offset:         96
        .size:           8
        .value_kind:     global_buffer
      - .actual_access:  read_only
        .address_space:  global
        .offset:         104
        .size:           8
        .value_kind:     global_buffer
      - .actual_access:  read_only
        .address_space:  global
        .offset:         112
        .size:           8
        .value_kind:     global_buffer
      - .actual_access:  write_only
        .address_space:  global
        .offset:         120
        .size:           8
        .value_kind:     global_buffer
      - .actual_access:  read_only
        .address_space:  global
        .offset:         128
        .size:           8
        .value_kind:     global_buffer
      - .address_space:  global
        .offset:         136
        .size:           8
        .value_kind:     global_buffer
      - .address_space:  global
        .offset:         144
        .size:           8
        .value_kind:     global_buffer
      - .address_space:  global
        .offset:         152
        .size:           8
        .value_kind:     global_buffer
      - .address_space:  global
        .offset:         160
        .size:           8
        .value_kind:     global_buffer
      - .address_space:  global
        .offset:         168
        .size:           8
        .value_kind:     global_buffer
      - .offset:         176
        .size:           4
        .value_kind:     hidden_block_count_x
      - .offset:         180
        .size:           4
        .value_kind:     hidden_block_count_y
      - .offset:         184
        .size:           4
        .value_kind:     hidden_block_count_z
      - .offset:         188
        .size:           2
        .value_kind:     hidden_group_size_x
      - .offset:         190
        .size:           2
        .value_kind:     hidden_group_size_y
      - .offset:         192
        .size:           2
        .value_kind:     hidden_group_size_z
      - .offset:         194
        .size:           2
        .value_kind:     hidden_remainder_x
      - .offset:         196
        .size:           2
        .value_kind:     hidden_remainder_y
      - .offset:         198
        .size:           2
        .value_kind:     hidden_remainder_z
      - .offset:         216
        .size:           8
        .value_kind:     hidden_global_offset_x
      - .offset:         224
        .size:           8
        .value_kind:     hidden_global_offset_y
      - .offset:         232
        .size:           8
        .value_kind:     hidden_global_offset_z
      - .offset:         240
        .size:           2
        .value_kind:     hidden_grid_dims
    .group_segment_fixed_size: 1024
    .kernarg_segment_align: 8
    .kernarg_segment_size: 432
    .language:       OpenCL C
    .language_version:
      - 2
      - 0
    .max_flat_workgroup_size: 1024
    .name:           _Z12prep_weightsPKfS0_S0_S0_S0_S0_S0_PDF16_S1_S1_S1_S0_S1_S0_S0_PfPKiPiS5_S5_S5_S5_
    .private_segment_fixed_size: 0
    .sgpr_count:     48
    .sgpr_spill_count: 0
    .symbol:         _Z12prep_weightsPKfS0_S0_S0_S0_S0_S0_PDF16_S1_S1_S1_S0_S1_S0_S0_PfPKiPiS5_S5_S5_S5_.kd
    .uniform_work_group_size: 1
    .uses_dynamic_stack: false
    .vgpr_count:     29
    .vgpr_spill_count: 0
    .wavefront_size: 64
  - .agpr_count:     0
    .args:
      - .actual_access:  read_only
        .address_space:  global
        .offset:         0
        .size:           8
        .value_kind:     global_buffer
      - .actual_access:  read_only
        .address_space:  global
        .offset:         8
        .size:           8
        .value_kind:     global_buffer
      - .actual_access:  read_only
        .address_space:  global
        .offset:         16
        .size:           8
        .value_kind:     global_buffer
      - .actual_access:  read_only
        .address_space:  global
        .offset:         24
        .size:           8
        .value_kind:     global_buffer
      - .actual_access:  read_only
        .address_space:  global
        .offset:         32
        .size:           8
        .value_kind:     global_buffer
      - .actual_access:  read_only
        .address_space:  global
        .offset:         40
        .size:           8
        .value_kind:     global_buffer
      - .actual_access:  read_only
        .address_space:  global
        .offset:         48
        .size:           8
        .value_kind:     global_buffer
      - .actual_access:  read_only
        .address_space:  global
        .offset:         56
        .size:           8
        .value_kind:     global_buffer
      - .actual_access:  write_only
        .address_space:  global
        .offset:         64
        .size:           8
        .value_kind:     global_buffer
      - .actual_access:  read_only
        .address_space:  global
        .offset:         72
        .size:           8
        .value_kind:     global_buffer
      - .actual_access:  read_only
        .address_space:  global
        .offset:         80
        .size:           8
        .value_kind:     global_buffer
      - .actual_access:  read_only
        .address_space:  global
        .offset:         88
        .size:           8
        .value_kind:     global_buffer
      - .actual_access:  read_only
        .address_space:  global
        .offset:         96
        .size:           8
        .value_kind:     global_buffer
      - .actual_access:  read_only
        .address_space:  global
        .offset:         104
        .size:           8
        .value_kind:     global_buffer
    .group_segment_fixed_size: 160832
    .kernarg_segment_align: 8
    .kernarg_segment_size: 112
    .language:       OpenCL C
    .language_version:
      - 2
      - 0
    .max_flat_workgroup_size: 512
    .name:           _Z8gru_mfmaPKiPKDF16_PKDv8_DF16_S5_S5_S5_S0_S0_PfPKfS8_S8_S8_S0_
    .private_segment_fixed_size: 0
    .sgpr_count:     27
    .sgpr_spill_count: 0
    .symbol:         _Z8gru_mfmaPKiPKDF16_PKDv8_DF16_S5_S5_S5_S0_S0_PfPKfS8_S8_S8_S0_.kd
    .uniform_work_group_size: 1
    .uses_dynamic_stack: false
    .vgpr_count:     256
    .vgpr_spill_count: 0
    .wavefront_size: 64
  - .agpr_count:     0
    .args:
      - .actual_access:  read_only
        .address_space:  global
        .offset:         0
        .size:           8
        .value_kind:     global_buffer
      - .actual_access:  read_only
        .address_space:  global
        .offset:         8
        .size:           8
        .value_kind:     global_buffer
      - .actual_access:  read_only
        .address_space:  global
        .offset:         16
        .size:           8
        .value_kind:     global_buffer
      - .actual_access:  read_only
        .address_space:  global
        .offset:         24
        .size:           8
        .value_kind:     global_buffer
      - .actual_access:  read_only
        .address_space:  global
        .offset:         32
        .size:           8
        .value_kind:     global_buffer
      - .actual_access:  read_only
        .address_space:  global
        .offset:         40
        .size:           8
        .value_kind:     global_buffer
      - .actual_access:  read_only
        .address_space:  global
        .offset:         48
        .size:           8
        .value_kind:     global_buffer
      - .actual_access:  read_only
        .address_space:  global
        .offset:         56
        .size:           8
        .value_kind:     global_buffer
      - .actual_access:  write_only
        .address_space:  global
        .offset:         64
        .size:           8
        .value_kind:     global_buffer
    .group_segment_fixed_size: 26624
    .kernarg_segment_align: 8
    .kernarg_segment_size: 72
    .language:       OpenCL C
    .language_version:
      - 2
      - 0
    .max_flat_workgroup_size: 256
    .name:           _Z10gcn_kernelPKiS0_S0_S0_PKfS2_S2_S2_Pf
    .private_segment_fixed_size: 0
    .sgpr_count:     42
    .sgpr_spill_count: 0
    .symbol:         _Z10gcn_kernelPKiS0_S0_S0_PKfS2_S2_S2_Pf.kd
    .uniform_work_group_size: 1
    .uses_dynamic_stack: false
    .vgpr_count:     96
    .vgpr_spill_count: 0
    .wavefront_size: 64
